# final plus non-temporal stores for the S5 input rows (ua) written by the input projection
# speedup vs baseline: 1.0078x; 1.0078x over previous
; DI u32x4 pack8(const f32x4& a, const f32x4& b) { u32x4 w; w.x = pk2(a[0], a[1]); w.y = pk2(a[2], a[3]); w.z = pk2(b[0], b[1]); w.w = pk2(b[2], b[3]); return w; }
;     DI void operator()(const f32x4 (&acc)[2][2][4][2], const Unit& u, int wr, int wc, int fr, int fq) const {
;         EPI_ROWS_BEGIN
;             const int row = u.pm * 256 + rt;
; #pragma unroll
;             for (int bj = 0; bj < 2; ++bj) { const int ch = u.pn * 256 + bj * 128 + 32 * wc + 8 * fq; const int g = ch >> 4, c0 = ch & 15;
;                 *(u32x4*)(ua + ((size_t)g * CROWS + (row >> 5)) * UAK + (row & 31) * 16 + c0) = pack8(acc[ai][bj][m][0] * sc, acc[ai][bj][m][1] * sc); }
;         EPI_ROWS_END
;     }
;     DI void operator()(const f32x4 (&acc)[2][2][4][2], const Unit& u, int wr, int wc, int fr, int fq) const {
;         Unit u2 = u;
;         if (u.pn < 2) { EpiScaled E{v, AW, sc}; E(acc, u2, wr, wc, fr, fq); }
;         else if (u.pn < 4) { u2.pn = u.pn - 2; EpiU E{ua, sc}; E(acc, u2, wr, wc, fr, fq); }
;         else { u2.pn = (u.pn - 4) & 3; EpiSig E{u.pn < 8 ? ga : gs, sc}; E(acc, u2, wr, wc, fr, fq); }
.LBB0_251:
	s_andn2_b64 vcc, exec, s[2:3]
	s_cbranch_vccnz .LBB0_253
	s_lshl_b32 s19, s21, 5
	v_lshlrev_b32_e32 v0, 4, v143
	s_lshl_b32 s29, s28, 8
	v_and_b32_e32 v0, 16, v0
	s_or_b32 s19, s29, s19
	v_lshl_add_u64 v[130:131], s[60:61], 0, v[0:1]
	v_lshlrev_b32_e32 v0, 5, v142
	s_addk_i32 s19, 0xfe00
	s_lshl_b32 s1, s23, 6
	s_lshl_b32 s0, s18, 8
	v_lshl_add_u64 v[134:135], v[130:131], 0, v[0:1]
	v_lshl_add_u32 v0, v143, 3, s19
	v_or_b32_e32 v156, s1, v142
	s_add_i32 s1, s1, s0
	v_ashrrev_i32_e32 v132, 4, v0
	s_ashr_i32 s2, s1, 5
	v_ashrrev_i32_e32 v133, 31, v132
	s_ashr_i32 s3, s2, 31
	v_pk_mul_f32 v[136:137], v[128:129], s[52:53] op_sel_hi:[1,0]
	v_pk_mul_f32 v[144:145], v[126:127], s[52:53] op_sel_hi:[1,0]
	v_lshlrev_b64 v[132:133], 10, v[132:133]
	v_pk_mul_f32 v[148:149], v[124:125], s[52:53] op_sel_hi:[1,0]
	v_pk_mul_f32 v[146:147], v[122:123], s[52:53] op_sel_hi:[1,0]
	v_cvt_pk_bf16_f32 v144, v144, v145
	v_cvt_pk_bf16_f32 v145, v136, v137
	v_lshl_add_u64 v[136:137], v[132:133], 0, s[2:3]
	s_movk_i32 s19, 0x500
	v_add_u32_e32 v0, 0x80, v0
	v_cvt_pk_bf16_f32 v146, v146, v147
	v_cvt_pk_bf16_f32 v147, v148, v149
	v_mad_u64_u32 v[148:149], s[30:31], v136, s19, v[134:135]
	v_ashrrev_i32_e32 v136, 4, v0
	v_mad_i32_i24 v149, v137, s19, v149
	v_ashrrev_i32_e32 v137, 31, v136
	global_store_dwordx4 v[148:149], v[144:147], off nt
	v_pk_mul_f32 v[150:151], v[108:109], s[52:53] op_sel_hi:[1,0]
	v_lshlrev_b64 v[136:137], 10, v[136:137]
	v_pk_mul_f32 v[146:147], v[116:117], s[52:53] op_sel_hi:[1,0]
	v_pk_mul_f32 v[144:145], v[114:115], s[52:53] op_sel_hi:[1,0]
	v_pk_mul_f32 v[152:153], v[106:107], s[52:53] op_sel_hi:[1,0]
	v_cvt_pk_bf16_f32 v144, v144, v145
	v_cvt_pk_bf16_f32 v145, v146, v147
	v_cvt_pk_bf16_f32 v147, v150, v151
	v_lshl_add_u64 v[150:151], v[136:137], 0, s[2:3]
	v_cvt_pk_bf16_f32 v146, v152, v153
	v_mad_u64_u32 v[152:153], s[30:31], v150, s19, v[134:135]
	v_mad_i32_i24 v153, v151, s19, v153
	global_store_dwordx4 v[152:153], v[144:147], off nt
	v_pk_mul_f32 v[150:151], v[112:113], s[52:53] op_sel_hi:[1,0]
	v_pk_mul_f32 v[154:155], v[110:111], s[52:53] op_sel_hi:[1,0]
	v_pk_mul_f32 v[146:147], v[120:121], s[52:53] op_sel_hi:[1,0]
	v_pk_mul_f32 v[144:145], v[118:119], s[52:53] op_sel_hi:[1,0]
	s_or_b32 s2, s2, 1
	v_cvt_pk_bf16_f32 v144, v144, v145
	v_cvt_pk_bf16_f32 v145, v146, v147
	v_cvt_pk_bf16_f32 v146, v154, v155
	v_cvt_pk_bf16_f32 v147, v150, v151
	global_store_dwordx4 v[148:149], v[144:147], off offset:512 nt
	v_pk_mul_f32 v[148:149], v[92:93], s[52:53] op_sel_hi:[1,0]
	v_pk_mul_f32 v[150:151], v[90:91], s[52:53] op_sel_hi:[1,0]
	v_pk_mul_f32 v[146:147], v[100:101], s[52:53] op_sel_hi:[1,0]
	v_pk_mul_f32 v[144:145], v[98:99], s[52:53] op_sel_hi:[1,0]
	s_ashr_i32 s3, s2, 31
	v_cvt_pk_bf16_f32 v144, v144, v145
	v_cvt_pk_bf16_f32 v145, v146, v147
	v_cvt_pk_bf16_f32 v146, v150, v151
	v_cvt_pk_bf16_f32 v147, v148, v149
	global_store_dwordx4 v[152:153], v[144:147], off offset:512 nt
	v_pk_mul_f32 v[148:149], v[96:97], s[52:53] op_sel_hi:[1,0]
	v_pk_mul_f32 v[150:151], v[94:95], s[52:53] op_sel_hi:[1,0]
	v_pk_mul_f32 v[146:147], v[104:105], s[52:53] op_sel_hi:[1,0]
	v_pk_mul_f32 v[144:145], v[102:103], s[52:53] op_sel_hi:[1,0]
	v_or_b32_e32 v0, 48, v156
	v_cvt_pk_bf16_f32 v144, v144, v145
	v_cvt_pk_bf16_f32 v145, v146, v147
	v_cvt_pk_bf16_f32 v147, v148, v149
	v_lshl_add_u64 v[148:149], v[132:133], 0, s[2:3]
	v_cvt_pk_bf16_f32 v146, v150, v151
	v_mad_u64_u32 v[150:151], s[30:31], v148, s19, v[134:135]
	v_mad_i32_i24 v151, v149, s19, v151
	global_store_dwordx4 v[150:151], v[144:147], off nt
	v_pk_mul_f32 v[148:149], v[76:77], s[52:53] op_sel_hi:[1,0]
	v_pk_mul_f32 v[150:151], v[74:75], s[52:53] op_sel_hi:[1,0]
	v_pk_mul_f32 v[146:147], v[84:85], s[52:53] op_sel_hi:[1,0]
	v_pk_mul_f32 v[144:145], v[82:83], s[52:53] op_sel_hi:[1,0]
	v_pk_mul_f32 v[152:153], v[80:81], s[52:53] op_sel_hi:[1,0]
	v_cvt_pk_bf16_f32 v144, v144, v145
	v_cvt_pk_bf16_f32 v145, v146, v147
	v_cvt_pk_bf16_f32 v147, v148, v149
	v_lshl_add_u64 v[148:149], v[136:137], 0, s[2:3]
	v_cvt_pk_bf16_f32 v146, v150, v151
	v_mad_u64_u32 v[150:151], s[2:3], v148, s19, v[134:135]
	v_mad_i32_i24 v151, v149, s19, v151
	global_store_dwordx4 v[150:151], v[144:147], off nt
	v_pk_mul_f32 v[154:155], v[78:79], s[52:53] op_sel_hi:[1,0]
	s_nop 0
	v_add_u32_e32 v144, s0, v0
	v_ashrrev_i32_e32 v148, 5, v144
	v_lshlrev_b32_e32 v0, 5, v0
	v_ashrrev_i32_e32 v149, 31, v148
	v_and_b32_e32 v0, 0x3e0, v0
	v_pk_mul_f32 v[146:147], v[88:89], s[52:53] op_sel_hi:[1,0]
	v_pk_mul_f32 v[144:145], v[86:87], s[52:53] op_sel_hi:[1,0]
	v_lshl_add_u64 v[150:151], v[130:131], 0, v[0:1]
	v_cvt_pk_bf16_f32 v144, v144, v145
	v_cvt_pk_bf16_f32 v145, v146, v147
	v_cvt_pk_bf16_f32 v147, v152, v153
	v_lshl_add_u64 v[152:153], v[132:133], 0, v[148:149]
	v_cvt_pk_bf16_f32 v146, v154, v155
	v_mad_u64_u32 v[154:155], s[2:3], v152, s19, v[150:151]
	v_lshl_add_u64 v[148:149], v[136:137], 0, v[148:149]
	v_mad_i32_i24 v155, v153, s19, v155
	v_mad_u64_u32 v[150:151], s[2:3], v148, s19, v[150:151]
	global_store_dwordx4 v[154:155], v[144:147], off nt
	v_pk_mul_f32 v[152:153], v[68:69], s[52:53] op_sel_hi:[1,0]
	v_pk_mul_f32 v[154:155], v[66:67], s[52:53] op_sel_hi:[1,0]
	v_pk_mul_f32 v[146:147], v[72:73], s[52:53] op_sel_hi:[1,0]
	v_pk_mul_f32 v[144:145], v[70:71], s[52:53] op_sel_hi:[1,0]
	s_add_i32 s2, s1, 0x80
	v_cvt_pk_bf16_f32 v144, v144, v145
	v_cvt_pk_bf16_f32 v145, v146, v147
	v_cvt_pk_bf16_f32 v146, v154, v155
; DI u32x4 pack8(const f32x4& a, const f32x4& b) { u32x4 w; w.x = pk2(a[0], a[1]); w.y = pk2(a[2], a[3]); w.z = pk2(b[0], b[1]); w.w = pk2(b[2], b[3]); return w; }
;     DI void operator()(const f32x4 (&acc)[2][2][4][2], const Unit& u, int wr, int wc, int fr, int fq) const {
;         EPI_ROWS_BEGIN
;             const int row = u.pm * 256 + rt;
; #pragma unroll
;             for (int bj = 0; bj < 2; ++bj) { const int ch = u.pn * 256 + bj * 128 + 32 * wc + 8 * fq; const int g = ch >> 4, c0 = ch & 15;
;                 *(u32x4*)(ua + ((size_t)g * CROWS + (row >> 5)) * UAK + (row & 31) * 16 + c0) = pack8(acc[ai][bj][m][0] * sc, acc[ai][bj][m][1] * sc); }
;         EPI_ROWS_END
	v_cvt_pk_bf16_f32 v147, v152, v153
	v_mad_i32_i24 v151, v149, s19, v151
	s_ashr_i32 s2, s2, 5
	global_store_dwordx4 v[150:151], v[144:147], off nt
	s_ashr_i32 s3, s2, 31
	v_pk_mul_f32 v[148:149], v[60:61], s[52:53] op_sel_hi:[1,0]
	v_pk_mul_f32 v[146:147], v[64:65], s[52:53] op_sel_hi:[1,0]
	v_pk_mul_f32 v[144:145], v[62:63], s[52:53] op_sel_hi:[1,0]
	v_pk_mul_f32 v[150:151], v[58:59], s[52:53] op_sel_hi:[1,0]
	v_cvt_pk_bf16_f32 v144, v144, v145
	v_cvt_pk_bf16_f32 v145, v146, v147
	v_cvt_pk_bf16_f32 v147, v148, v149
	v_lshl_add_u64 v[148:149], v[132:133], 0, s[2:3]
	v_cvt_pk_bf16_f32 v146, v150, v151
	v_mad_u64_u32 v[150:151], s[30:31], v148, s19, v[134:135]
	v_mad_i32_i24 v151, v149, s19, v151
	global_store_dwordx4 v[150:151], v[144:147], off nt
	v_pk_mul_f32 v[148:149], v[44:45], s[52:53] op_sel_hi:[1,0]
	v_pk_mul_f32 v[150:151], v[42:43], s[52:53] op_sel_hi:[1,0]
	v_pk_mul_f32 v[146:147], v[52:53], s[52:53] op_sel_hi:[1,0]
	v_pk_mul_f32 v[144:145], v[50:51], s[52:53] op_sel_hi:[1,0]
	v_add_u32_e32 v0, 0x90, v156
	v_cvt_pk_bf16_f32 v144, v144, v145
	v_cvt_pk_bf16_f32 v145, v146, v147
	v_cvt_pk_bf16_f32 v147, v148, v149
	v_lshl_add_u64 v[148:149], v[136:137], 0, s[2:3]
	v_cvt_pk_bf16_f32 v146, v150, v151
	v_mad_u64_u32 v[150:151], s[2:3], v148, s19, v[134:135]
	v_mad_i32_i24 v151, v149, s19, v151
	global_store_dwordx4 v[150:151], v[144:147], off nt
	v_pk_mul_f32 v[152:153], v[48:49], s[52:53] op_sel_hi:[1,0]
	v_pk_mul_f32 v[154:155], v[46:47], s[52:53] op_sel_hi:[1,0]
	v_add_u32_e32 v144, s0, v0
	v_ashrrev_i32_e32 v148, 5, v144
	v_lshlrev_b32_e32 v0, 5, v0
	v_ashrrev_i32_e32 v149, 31, v148
	v_and_b32_e32 v0, 0x3e0, v0
	v_pk_mul_f32 v[146:147], v[56:57], s[52:53] op_sel_hi:[1,0]
	v_pk_mul_f32 v[144:145], v[54:55], s[52:53] op_sel_hi:[1,0]
	v_lshl_add_u64 v[150:151], v[130:131], 0, v[0:1]
	v_cvt_pk_bf16_f32 v144, v144, v145
	v_cvt_pk_bf16_f32 v145, v146, v147
	v_cvt_pk_bf16_f32 v147, v152, v153
	v_lshl_add_u64 v[152:153], v[132:133], 0, v[148:149]
	v_cvt_pk_bf16_f32 v146, v154, v155
	v_mad_u64_u32 v[154:155], s[2:3], v152, s19, v[150:151]
	v_mad_i32_i24 v155, v153, s19, v155
	v_lshl_add_u64 v[148:149], v[136:137], 0, v[148:149]
	global_store_dwordx4 v[154:155], v[144:147], off nt
	v_pk_mul_f32 v[152:153], v[28:29], s[52:53] op_sel_hi:[1,0]
	v_pk_mul_f32 v[154:155], v[26:27], s[52:53] op_sel_hi:[1,0]
	v_pk_mul_f32 v[146:147], v[36:37], s[52:53] op_sel_hi:[1,0]
	v_pk_mul_f32 v[144:145], v[34:35], s[52:53] op_sel_hi:[1,0]
	v_mad_u64_u32 v[150:151], s[2:3], v148, s19, v[150:151]
	s_addk_i32 s1, 0xa0
	v_cvt_pk_bf16_f32 v144, v144, v145
	v_cvt_pk_bf16_f32 v145, v146, v147
	v_cvt_pk_bf16_f32 v146, v154, v155
	v_cvt_pk_bf16_f32 v147, v152, v153
	v_mad_i32_i24 v151, v149, s19, v151
	s_ashr_i32 s2, s1, 5
	global_store_dwordx4 v[150:151], v[144:147], off nt
	s_ashr_i32 s3, s2, 31
	v_pk_mul_f32 v[148:149], v[32:33], s[52:53] op_sel_hi:[1,0]
	v_pk_mul_f32 v[146:147], v[40:41], s[52:53] op_sel_hi:[1,0]
	v_pk_mul_f32 v[144:145], v[38:39], s[52:53] op_sel_hi:[1,0]
	v_pk_mul_f32 v[150:151], v[30:31], s[52:53] op_sel_hi:[1,0]
	v_cvt_pk_bf16_f32 v144, v144, v145
	v_cvt_pk_bf16_f32 v145, v146, v147
	v_cvt_pk_bf16_f32 v147, v148, v149
	v_lshl_add_u64 v[148:149], v[132:133], 0, s[2:3]
	v_cvt_pk_bf16_f32 v146, v150, v151
	v_mad_u64_u32 v[150:151], s[30:31], v148, s19, v[134:135]
	v_mad_i32_i24 v151, v149, s19, v151
	global_store_dwordx4 v[150:151], v[144:147], off nt
	v_pk_mul_f32 v[148:149], v[12:13], s[52:53] op_sel_hi:[1,0]
	v_pk_mul_f32 v[150:151], v[10:11], s[52:53] op_sel_hi:[1,0]
	v_pk_mul_f32 v[146:147], v[20:21], s[52:53] op_sel_hi:[1,0]
	v_pk_mul_f32 v[144:145], v[18:19], s[52:53] op_sel_hi:[1,0]
	v_add_u32_e32 v0, 0xb0, v156
	v_cvt_pk_bf16_f32 v144, v144, v145
	v_cvt_pk_bf16_f32 v145, v146, v147
	v_cvt_pk_bf16_f32 v147, v148, v149
	v_lshl_add_u64 v[148:149], v[136:137], 0, s[2:3]
	v_mad_u64_u32 v[134:135], s[2:3], v148, s19, v[134:135]
	v_cvt_pk_bf16_f32 v146, v150, v151
	v_mad_i32_i24 v135, v149, s19, v135
	global_store_dwordx4 v[134:135], v[144:147], off nt
	v_add_u32_e32 v134, s0, v0
	v_lshlrev_b32_e32 v0, 5, v0
	v_ashrrev_i32_e32 v134, 5, v134
	v_and_b32_e32 v0, 0x3e0, v0
	v_ashrrev_i32_e32 v135, 31, v134
	v_lshl_add_u64 v[148:149], v[130:131], 0, v[0:1]
	v_pk_mul_f32 v[130:131], v[24:25], s[52:53] op_sel_hi:[1,0]
	v_pk_mul_f32 v[144:145], v[22:23], s[52:53] op_sel_hi:[1,0]
	v_pk_mul_f32 v[150:151], v[16:17], s[52:53] op_sel_hi:[1,0]
	v_cvt_pk_bf16_f32 v144, v144, v145
	v_cvt_pk_bf16_f32 v145, v130, v131
	v_lshl_add_u64 v[130:131], v[132:133], 0, v[134:135]
	v_pk_mul_f32 v[146:147], v[14:15], s[52:53] op_sel_hi:[1,0]
	v_mad_u64_u32 v[132:133], s[0:1], v130, s19, v[148:149]
	v_cvt_pk_bf16_f32 v146, v146, v147
	v_cvt_pk_bf16_f32 v147, v150, v151
	v_mad_i32_i24 v133, v131, s19, v133
	v_lshl_add_u64 v[134:135], v[136:137], 0, v[134:135]
	global_store_dwordx4 v[132:133], v[144:147], off nt
	v_pk_mul_f32 v[132:133], v[8:9], s[52:53] op_sel_hi:[1,0]
	v_pk_mul_f32 v[130:131], v[6:7], s[52:53] op_sel_hi:[1,0]
	v_pk_mul_f32 v[144:145], v[4:5], s[52:53] op_sel_hi:[1,0]
	v_pk_mul_f32 v[146:147], v[2:3], s[52:53] op_sel_hi:[1,0]
	v_mad_u64_u32 v[136:137], s[0:1], v134, s19, v[148:149]
	v_cvt_pk_bf16_f32 v130, v130, v131
	v_cvt_pk_bf16_f32 v131, v132, v133
	v_cvt_pk_bf16_f32 v132, v146, v147
	v_cvt_pk_bf16_f32 v133, v144, v145
	v_mad_i32_i24 v137, v135, s19, v137
	global_store_dwordx4 v[136:137], v[130:133], off nt
